# P0 LRU gate-weight conversion: 8 strided loads per thread in flight (was 16 dependent round trips); plus previous unit-boundary and prologue trims
# speedup vs baseline: 1.0105x; 1.0048x over previous
.LBB0_191:
	s_load_dwordx2 s[6:7], s[0:1], 0x60
	s_load_dwordx2 s[14:15], s[0:1], 0x70
	v_lshrrev_b32_e32 v4, 14, v6
	v_and_b32_e32 v4, 7, v4
	v_and_b32_e32 v9, 0x7f, v6
	v_lshlrev_b32_e32 v9, 9, v9
	v_lshl_add_u32 v4, v4, 16, v9
	v_bfe_u32 v9, v6, 7, 7
	v_lshl_add_u32 v4, v9, 2, v4
	s_waitcnt lgkmcnt(0)
	global_load_dword v10, v4, s[6:7]
	global_load_dword v11, v4, s[14:15]
	s_add_u32 s6, s6, 0x80000
	s_addc_u32 s7, s7, 0
	s_add_u32 s14, s14, 0x80000
	s_addc_u32 s15, s15, 0
	global_load_dword v12, v4, s[6:7]
	global_load_dword v13, v4, s[14:15]
	s_add_u32 s6, s6, 0x80000
	s_addc_u32 s7, s7, 0
	s_add_u32 s14, s14, 0x80000
	s_addc_u32 s15, s15, 0
	global_load_dword v14, v4, s[6:7]
	global_load_dword v15, v4, s[14:15]
	s_add_u32 s6, s6, 0x80000
	s_addc_u32 s7, s7, 0
	s_add_u32 s14, s14, 0x80000
	s_addc_u32 s15, s15, 0
	global_load_dword v16, v4, s[6:7]
	global_load_dword v17, v4, s[14:15]
	s_waitcnt vmcnt(7)
	v_bfe_u32 v9, v10, 16, 1
	v_add3_u32 v10, v10, v9, s17
	global_store_short_d16_hi v[2:3], v10, off
	v_lshl_add_u64 v[2:3], v[2:3], 0, s[8:9]
	s_waitcnt vmcnt(7)
	v_bfe_u32 v9, v11, 16, 1
	v_add3_u32 v11, v11, v9, s17
	global_store_short_d16_hi v[2:3], v11, off
	v_lshl_add_u64 v[2:3], v[2:3], 0, s[8:9]
	s_waitcnt vmcnt(7)
	v_bfe_u32 v9, v12, 16, 1
	v_add3_u32 v12, v12, v9, s17
	global_store_short_d16_hi v[2:3], v12, off
	v_lshl_add_u64 v[2:3], v[2:3], 0, s[8:9]
	s_waitcnt vmcnt(7)
	v_bfe_u32 v9, v13, 16, 1
	v_add3_u32 v13, v13, v9, s17
	global_store_short_d16_hi v[2:3], v13, off
	v_lshl_add_u64 v[2:3], v[2:3], 0, s[8:9]
	s_waitcnt vmcnt(7)
	v_bfe_u32 v9, v14, 16, 1
	v_add3_u32 v14, v14, v9, s17
	global_store_short_d16_hi v[2:3], v14, off
	v_lshl_add_u64 v[2:3], v[2:3], 0, s[8:9]
	s_waitcnt vmcnt(7)
	v_bfe_u32 v9, v15, 16, 1
	v_add3_u32 v15, v15, v9, s17
	global_store_short_d16_hi v[2:3], v15, off
	v_lshl_add_u64 v[2:3], v[2:3], 0, s[8:9]
	s_waitcnt vmcnt(7)
	v_bfe_u32 v9, v16, 16, 1
	v_add3_u32 v16, v16, v9, s17
	global_store_short_d16_hi v[2:3], v16, off
	v_lshl_add_u64 v[2:3], v[2:3], 0, s[8:9]
	s_waitcnt vmcnt(7)
	v_bfe_u32 v9, v17, 16, 1
	v_add3_u32 v17, v17, v9, s17
	global_store_short_d16_hi v[2:3], v17, off
	v_lshl_add_u64 v[2:3], v[2:3], 0, s[8:9]
